# L2 warm-up at the XCD-local barrier before w1/w2: idle waves 1-7 touch (sc1, discarded) the first two K-tiles of the workgroup's weight panel (w2: also A panel) so the GEMM prologue hits L2 (on v16)
# speedup vs baseline: 1.0067x; 1.0067x over previous
.LBB0_1159:
	s_and_b64 vcc, exec, s[0:1]
	s_cbranch_vccz .LBB0_1178
	v_readlane_b32 s0, v255, 10
	s_waitcnt vmcnt(0)
	s_add_i32 s0, s0, 1
	s_waitcnt vmcnt(0) lgkmcnt(0)
	v_writelane_b32 v255, s0, 10
	s_barrier
	v_readlane_b32 s100, v254, 6
	v_readlane_b32 s101, v254, 0
	v_mbcnt_lo_u32_b32 v253, -1, 0
	v_mbcnt_hi_u32_b32 v253, -1, v253
	s_nop 1
	s_cmp_eq_u32 s100, 0
	s_cbranch_scc1 .Lpf_w1_skip
	s_add_i32 s100, s100, -1
	s_lshl_b32 s100, s100, 13
	v_lshl_add_u32 v253, v253, 7, s100
	s_lshr_b32 s100, s101, 5
	s_lshl_b32 s100, s100, 20
	s_lshl_b32 s101, s36, 25
	s_add_i32 s100, s100, s101
	s_add_i32 s100, s100, 0x8100000
	v_add_u32_e32 v252, s100, v253
	global_load_dword v252, v252, s[82:83] sc1
.Lpf_w1_skip:
	s_mov_b64 s[0:1], exec
	v_readlane_b32 s8, v254, 4
	v_readlane_b32 s9, v254, 5
	s_and_b64 s[8:9], s[0:1], s[8:9]
	s_mov_b64 exec, s[8:9]
	s_cbranch_execz .LBB0_1177
	s_mov_b64 s[8:9], exec
	v_mbcnt_lo_u32_b32 v1, s8, 0
	v_mbcnt_hi_u32_b32 v1, s9, v1
	v_cmp_eq_u32_e32 vcc, 0, v1
	s_waitcnt vmcnt(0) expcnt(0) lgkmcnt(0)
	s_and_saveexec_b64 s[10:11], vcc
	s_cbranch_execz .LBB0_1163
	s_bcnt1_i32_b64 s7, s[8:9]
	v_readlane_b32 s8, v254, 51
	v_mov_b32_e32 v1, s7
	v_readlane_b32 s9, v254, 52
	s_nop 4
	global_atomic_add v115, v1, s[8:9] offset:2048

.LBB0_1294:
	s_and_b64 vcc, exec, s[0:1]
	s_cbranch_vccz .LBB0_1313
	v_readlane_b32 s0, v255, 10
	s_waitcnt vmcnt(0)
	s_add_i32 s0, s0, 1
	s_waitcnt vmcnt(0) lgkmcnt(0)
	v_writelane_b32 v255, s0, 10
	s_barrier
	v_readlane_b32 s100, v254, 6
	v_readlane_b32 s101, v254, 0
	v_mbcnt_lo_u32_b32 v253, -1, 0
	v_mbcnt_hi_u32_b32 v253, -1, v253
	s_nop 1
	s_cmp_eq_u32 s100, 0
	s_cbranch_scc1 .Lpf_w2_skip
	s_add_i32 s100, s100, -1
	s_lshl_b32 s100, s100, 13
	v_lshl_add_u32 v253, v253, 7, s100
	s_lshr_b32 s100, s101, 5
	s_lshl_b32 s100, s100, 22
	s_lshl_b32 s101, s36, 25
	s_add_i32 s100, s100, s101
	s_add_i32 s100, s100, 0x10100000
	v_add_u32_e32 v252, s100, v253
	global_load_dword v252, v252, s[82:83] sc1
	v_readlane_b32 s101, v254, 0
	s_nop 1
	s_and_b32 s100, s101, 7
	s_lshl_b32 s100, s100, 2
	s_bfe_u32 s101, s101, 0x20003
	s_or_b32 s100, s100, s101
	s_lshl_b32 s100, s100, 22
	s_add_i32 s100, s100, 0x28100000
	v_add_u32_e32 v251, s100, v253
	global_load_dword v251, v251, s[82:83] sc1
.Lpf_w2_skip:
	s_mov_b64 s[0:1], exec
	v_readlane_b32 s4, v254, 4
	v_readlane_b32 s5, v254, 5
	s_and_b64 s[4:5], s[0:1], s[4:5]
	s_mov_b64 exec, s[4:5]
	s_cbranch_execz .LBB0_1312
	s_mov_b64 s[4:5], exec
	v_mbcnt_lo_u32_b32 v1, s4, 0
	v_mbcnt_hi_u32_b32 v1, s5, v1
	v_cmp_eq_u32_e32 vcc, 0, v1
	s_waitcnt vmcnt(0) expcnt(0) lgkmcnt(0)
	s_and_saveexec_b64 s[8:9], vcc
	s_cbranch_execz .LBB0_1298
	s_bcnt1_i32_b64 s4, s[4:5]
	v_mov_b32_e32 v1, s4
	v_readlane_b32 s4, v254, 51
	v_readlane_b32 s5, v254, 52
	s_nop 4
	global_atomic_add v115, v1, s[4:5] offset:2048
